# QK^T section: third K-fragment pair read behind the first two MFMAs into the spare register pair, fourth pair behind MFMA 3/4; waits 2/2/2/0, each with two MFMAs of distance, no larger read burst at t
# speedup vs baseline: 1.0042x; 1.0042x over previous
.LBB0_787:
	ds_read_b128 v[80:83], v134 offset:33792
	ds_read_b128 v[84:87], v134 offset:41984
	ds_read_b128 v[196:199], v135 offset:33792
	ds_read_b128 v[200:203], v135 offset:41984
	s_waitcnt lgkmcnt(2)
	v_mfma_f32_32x32x16_bf16 v[96:111], v[80:83], v[122:125], 0
	v_exp_f32_e32 v204, v72
	v_exp_f32_e32 v205, v73
	v_exp_f32_e32 v206, v74
	v_exp_f32_e32 v207, v75
	v_exp_f32_e32 v208, v76
	v_exp_f32_e32 v209, v77
	v_mfma_f32_32x32x16_bf16 v[80:95], v[84:87], v[122:125], 0
	ds_read_b128 v[138:141], v136 offset:33792
	ds_read_b128 v[142:145], v136 offset:41984
	v_exp_f32_e32 v210, v78
	v_exp_f32_e32 v79, v79
	s_waitcnt lgkmcnt(2)
	v_mfma_f32_32x32x16_bf16 v[96:111], v[196:199], v[126:129], v[96:111]
	v_mfma_f32_32x32x16_bf16 v[80:95], v[200:203], v[126:129], v[80:95]
	ds_read_b128 v[196:199], v137 offset:33792
	ds_read_b128 v[200:203], v137 offset:41984
	s_waitcnt lgkmcnt(2)
	v_mfma_f32_32x32x16_bf16 v[96:111], v[138:141], v[118:121], v[96:111]
	v_mfma_f32_32x32x16_bf16 v[80:95], v[142:145], v[118:121], v[80:95]
	v_exp_f32_e32 v180, v64
	v_add_f32_e32 v64, v161, v159
	v_add_f32_e32 v195, v157, v160
	v_add_f32_e32 v64, v155, v64
	v_add_f32_e32 v195, v158, v195
	v_add_f32_e32 v64, v154, v64
	v_add_f32_e32 v195, v156, v195
	v_add_f32_e32 v64, v151, v64
	v_add_f32_e32 v195, v153, v195
	v_add_f32_e32 v64, v149, v64
	v_add_f32_e32 v195, v152, v195
	v_add_f32_e32 v64, v147, v64
	s_waitcnt lgkmcnt(0)
	v_mfma_f32_32x32x16_bf16 v[96:111], v[196:199], v[114:117], v[96:111]
	v_exp_f32_e32 v197, v65
	v_add_f32_e32 v195, v150, v195
	v_exp_f32_e32 v198, v66
	v_add_f32_e32 v64, v146, v64
	v_exp_f32_e32 v199, v67
	v_add_f32_e32 v195, v148, v195
	v_add_f32_e32 v64, v180, v64
	v_mfma_f32_32x32x16_bf16 v[80:95], v[200:203], v[114:117], v[80:95]
	v_exp_f32_e32 v200, v68
	v_exp_f32_e32 v201, v69
	v_add_f32_e32 v195, v197, v195
	v_exp_f32_e32 v202, v70
	v_add_f32_e32 v64, v198, v64
	v_exp_f32_e32 v203, v71
	v_add_f32_e32 v195, v199, v195
	v_add_f32_e32 v64, v200, v64
	v_add_f32_e32 v195, v201, v195
	v_add_f32_e32 v64, v202, v64
	v_add_f32_e32 v195, v203, v195
	v_add_f32_e32 v64, v204, v64
	v_add_f32_e32 v195, v205, v195
	v_add_f32_e32 v64, v206, v64
	v_add_f32_e32 v195, v207, v195
	v_add_f32_e32 v64, v208, v64
	v_add_f32_e32 v195, v209, v195
	v_add_f32_e32 v64, v210, v64
	v_add_f32_e32 v195, v79, v195
	v_add_f32_e32 v195, v195, v64
	v_cvt_pk_bf16_f32 v64, v159, v161
	v_cvt_pk_bf16_f32 v65, v157, v160
	v_cvt_pk_bf16_f32 v66, v155, v158
	v_cvt_pk_bf16_f32 v67, v154, v156
	v_cvt_pk_bf16_f32 v68, v151, v153
	v_cvt_pk_bf16_f32 v69, v149, v152
	v_cvt_pk_bf16_f32 v70, v147, v150
	v_cvt_pk_bf16_f32 v71, v146, v148
	v_cvt_pk_bf16_f32 v72, v180, v197
	v_cvt_pk_bf16_f32 v73, v198, v199
	v_cvt_pk_bf16_f32 v74, v200, v201
	v_cvt_pk_bf16_f32 v75, v202, v203
	v_cvt_pk_bf16_f32 v76, v204, v205
	v_cvt_pk_bf16_f32 v77, v206, v207
	v_cvt_pk_bf16_f32 v78, v208, v209
	v_cvt_pk_bf16_f32 v79, v210, v79
	s_add_i32 m0, s84, 0x8400
	s_add_u32 s66, s78, s65
	s_addc_u32 s67, s79, 0
	global_load_lds_dwordx4 v185, s[66:67]
	s_add_i32 m0, s84, 0xa400
	s_add_i32 s64, s65, 0x60000
	global_load_lds_dwordx4 v184, s[66:67]
	s_add_i32 m0, s84, 0xc400
	s_add_u32 s70, s80, s64
	s_addc_u32 s71, s81, 0
	global_load_lds_dwordx4 v183, s[70:71]
	s_add_i32 m0, s84, 0xe400
	s_mov_b32 s65, s64
	global_load_lds_dwordx4 v182, s[70:71]
	ds_read_b64_tr_b16 v[198:199], v192 offset:1024
	ds_read_b64_tr_b16 v[200:201], v192 offset:3072
	ds_read_b64_tr_b16 v[202:203], v192 offset:5120
	ds_read_b64_tr_b16 v[204:205], v192 offset:7168
	ds_read_b64_tr_b16 v[206:207], v192 offset:9216
	ds_read_b64_tr_b16 v[208:209], v192 offset:11264
	ds_read_b64_tr_b16 v[222:223], v192 offset:13312
	ds_read_b64_tr_b16 v[224:225], v192 offset:15360
	s_waitcnt lgkmcnt(0)
	v_mfma_f32_32x32x16_bf16 v[0:15], v[64:67], v[198:201], v[0:15]
	ds_read_b64_tr_b16 v[198:199], v192 offset:1536
	ds_read_b64_tr_b16 v[200:201], v192 offset:3584
	ds_read_b64_tr_b16 v[138:139], v192 offset:9728
	ds_read_b64_tr_b16 v[140:141], v192 offset:11776
	v_mfma_f32_32x32x16_bf16 v[0:15], v[68:71], v[202:205], v[0:15]
	ds_read_b64_tr_b16 v[202:203], v192 offset:5632
	ds_read_b64_tr_b16 v[204:205], v192 offset:7680
	ds_read_b64_tr_b16 v[142:143], v192 offset:13824
	ds_read_b64_tr_b16 v[144:145], v192 offset:15872
	v_mfma_f32_32x32x16_bf16 v[0:15], v[72:75], v[206:209], v[0:15]
	v_mfma_f32_32x32x16_bf16 v[0:15], v[76:79], v[222:225], v[0:15]
	s_waitcnt lgkmcnt(0)
	v_mfma_f32_32x32x16_bf16 v[48:63], v[64:67], v[198:201], v[48:63]
	ds_read_b64_tr_b16 v[198:199], v192 offset:2048
	ds_read_b64_tr_b16 v[200:201], v192 offset:4096
	ds_read_b64_tr_b16 v[206:207], v192 offset:10240
	ds_read_b64_tr_b16 v[208:209], v192 offset:12288
	v_mfma_f32_32x32x16_bf16 v[48:63], v[68:71], v[202:205], v[48:63]
	ds_read_b64_tr_b16 v[202:203], v192 offset:6144
	ds_read_b64_tr_b16 v[204:205], v192 offset:8192
	ds_read_b64_tr_b16 v[222:223], v192 offset:14336
	ds_read_b64_tr_b16 v[224:225], v192 offset:16384
	v_mfma_f32_32x32x16_bf16 v[48:63], v[72:75], v[138:141], v[48:63]
	v_mfma_f32_32x32x16_bf16 v[48:63], v[76:79], v[142:145], v[48:63]
	s_waitcnt lgkmcnt(0)
	v_mfma_f32_32x32x16_bf16 v[32:47], v[64:67], v[198:201], v[32:47]
	ds_read_b64_tr_b16 v[198:199], v192 offset:2560
	ds_read_b64_tr_b16 v[200:201], v192 offset:4608
	ds_read_b64_tr_b16 v[138:139], v192 offset:10752
	ds_read_b64_tr_b16 v[140:141], v192 offset:12800
	v_mfma_f32_32x32x16_bf16 v[32:47], v[68:71], v[202:205], v[32:47]
	ds_read_b64_tr_b16 v[202:203], v192 offset:6656
	ds_read_b64_tr_b16 v[204:205], v192 offset:8704
	ds_read_b64_tr_b16 v[142:143], v192 offset:14848
	ds_read_b64_tr_b16 v[144:145], v192 offset:16896
	v_mfma_f32_32x32x16_bf16 v[32:47], v[72:75], v[206:209], v[32:47]
	v_mfma_f32_32x32x16_bf16 v[32:47], v[76:79], v[222:225], v[32:47]
	s_waitcnt lgkmcnt(0)
	v_mfma_f32_32x32x16_bf16 v[16:31], v[64:67], v[198:201], v[16:31]
	v_max_f32_e32 v64, v96, v97
	v_max3_f32 v65, v80, v81, v82
	v_max3_f32 v64, v64, v98, v99
	v_max3_f32 v65, v65, v83, v84
	v_max3_f32 v64, v64, v100, v101
	v_mfma_f32_32x32x16_bf16 v[16:31], v[68:71], v[202:205], v[16:31]
	v_max3_f32 v65, v65, v85, v86
	v_max3_f32 v64, v64, v102, v103
	v_max3_f32 v65, v65, v87, v88
	v_max3_f32 v64, v64, v104, v105
	v_max3_f32 v65, v65, v89, v90
	v_max3_f32 v64, v64, v106, v107
	v_max3_f32 v65, v65, v91, v92
	v_mfma_f32_32x32x16_bf16 v[16:31], v[72:75], v[138:141], v[16:31]
	v_max3_f32 v64, v64, v108, v109
	v_max3_f32 v65, v65, v93, v94
	v_max3_f32 v64, v64, v110, v111
	v_max3_f32 v64, v64, v65, v95
	v_mov_b32_e32 v198, 1.0
	v_mfma_f32_32x32x16_bf16 v[16:31], v[76:79], v[142:145], v[16:31]
	v_cmp_ge_f32_e64 s[0:1], s56, v64
	s_cmp_eq_u64 s[0:1], exec
	s_cbranch_scc1 .LBB0_792
	s_branch .LBB0_801

.LBB0_792:
	v_exp_f32_e32 v197, v96
	v_exp_f32_e32 v208, v97
	v_exp_f32_e32 v209, v98
	v_exp_f32_e32 v210, v99
	v_exp_f32_e32 v211, v100
	v_exp_f32_e32 v220, v101
	v_exp_f32_e32 v221, v102
	v_exp_f32_e32 v222, v103
	v_exp_f32_e32 v223, v104
	v_exp_f32_e32 v224, v105
	v_exp_f32_e32 v225, v106
	v_exp_f32_e32 v226, v107
	v_exp_f32_e32 v227, v108
	v_exp_f32_e32 v228, v109
	v_exp_f32_e32 v229, v110
	v_exp_f32_e32 v230, v111
	s_waitcnt vmcnt(4) lgkmcnt(0)
	s_barrier
	ds_read_b128 v[64:67], v134 offset:50176
	ds_read_b128 v[68:71], v134 offset:58368
	ds_read_b128 v[200:203], v135 offset:50176
	ds_read_b128 v[204:207], v135 offset:58368
	v_exp_f32_e32 v231, v87
	s_waitcnt lgkmcnt(2)
	v_mfma_f32_32x32x16_bf16 v[96:111], v[64:67], v[122:125], 0
	v_exp_f32_e32 v232, v88
	v_exp_f32_e32 v233, v89
	v_exp_f32_e32 v234, v90
	v_exp_f32_e32 v235, v91
	v_exp_f32_e32 v236, v92
	v_exp_f32_e32 v237, v93
	v_exp_f32_e32 v238, v94
	v_mfma_f32_32x32x16_bf16 v[64:79], v[68:71], v[122:125], 0
	ds_read_b128 v[138:141], v136 offset:50176
	ds_read_b128 v[142:145], v136 offset:58368
	v_exp_f32_e32 v95, v95
	s_waitcnt lgkmcnt(2)
	v_mfma_f32_32x32x16_bf16 v[96:111], v[200:203], v[126:129], v[96:111]
	v_mfma_f32_32x32x16_bf16 v[64:79], v[204:207], v[126:129], v[64:79]
	ds_read_b128 v[200:203], v137 offset:50176
	ds_read_b128 v[204:207], v137 offset:58368
	s_waitcnt lgkmcnt(2)
	v_mfma_f32_32x32x16_bf16 v[96:111], v[138:141], v[118:121], v[96:111]
	v_mfma_f32_32x32x16_bf16 v[64:79], v[142:145], v[118:121], v[64:79]
	s_waitcnt lgkmcnt(0)
	v_mfma_f32_32x32x16_bf16 v[96:111], v[200:203], v[114:117], v[96:111]
	v_exp_f32_e32 v201, v80
	v_add_f32_e32 v80, v208, v197
	v_add_f32_e32 v199, v209, v210
	v_add_f32_e32 v80, v211, v80
	v_add_f32_e32 v199, v220, v199
	v_add_f32_e32 v80, v221, v80
	v_add_f32_e32 v199, v222, v199
	v_add_f32_e32 v80, v223, v80
	v_add_f32_e32 v199, v224, v199
	v_add_f32_e32 v80, v225, v80
	v_add_f32_e32 v199, v226, v199
	v_add_f32_e32 v80, v227, v80
	v_exp_f32_e32 v202, v81
	v_add_f32_e32 v199, v228, v199
	v_exp_f32_e32 v203, v82
	v_add_f32_e32 v80, v229, v80
	v_mfma_f32_32x32x16_bf16 v[64:79], v[204:207], v[114:117], v[64:79]
	v_exp_f32_e32 v204, v83
	v_add_f32_e32 v199, v230, v199
	v_exp_f32_e32 v205, v84
	v_add_f32_e32 v80, v201, v80
	v_exp_f32_e32 v206, v85
	v_add_f32_e32 v199, v202, v199
	v_exp_f32_e32 v207, v86
	v_add_f32_e32 v80, v203, v80
	v_add_f32_e32 v199, v204, v199
	v_add_f32_e32 v80, v205, v80
	v_add_f32_e32 v199, v206, v199
	v_add_f32_e32 v80, v207, v80
	v_add_f32_e32 v199, v231, v199
	v_add_f32_e32 v80, v232, v80
	v_add_f32_e32 v199, v233, v199
	v_add_f32_e32 v80, v234, v80
	v_add_f32_e32 v199, v235, v199
	v_add_f32_e32 v80, v236, v80
	v_add_f32_e32 v199, v237, v199
	v_add_f32_e32 v80, v238, v80
	v_add_f32_e32 v199, v95, v199
	v_add_f32_e32 v199, v199, v80
	v_cvt_pk_bf16_f32 v80, v197, v208
	v_cvt_pk_bf16_f32 v81, v209, v210
	v_cvt_pk_bf16_f32 v82, v211, v220
	v_cvt_pk_bf16_f32 v83, v221, v222
	v_cvt_pk_bf16_f32 v84, v223, v224
	v_cvt_pk_bf16_f32 v85, v225, v226
	v_cvt_pk_bf16_f32 v86, v227, v228
	v_cvt_pk_bf16_f32 v87, v229, v230
	v_cvt_pk_bf16_f32 v88, v201, v202
	v_cvt_pk_bf16_f32 v89, v203, v204
	v_cvt_pk_bf16_f32 v90, v205, v206
	v_cvt_pk_bf16_f32 v91, v207, v231
	v_cvt_pk_bf16_f32 v92, v232, v233
	v_cvt_pk_bf16_f32 v93, v234, v235
	v_cvt_pk_bf16_f32 v94, v236, v237
	v_cvt_pk_bf16_f32 v95, v238, v95
	s_add_i32 m0, s84, 0x400
	s_add_u32 s66, s78, s65
	s_addc_u32 s67, s79, 0
	global_load_lds_dwordx4 v185, s[66:67]
	s_add_i32 m0, s84, 0x2400
	s_add_i32 s64, s65, 0x60000
	global_load_lds_dwordx4 v184, s[66:67]
	s_cmp_eq_u32 s55, 29
	s_cselect_b32 s64, s89, s64
	s_add_i32 m0, s84, 0x10400
	s_add_u32 s70, s80, s64
	s_addc_u32 s71, s81, 0
	global_load_lds_dwordx4 v183, s[70:71]
	s_add_i32 m0, s84, 0x12400
	s_mov_b32 s65, s64
	global_load_lds_dwordx4 v182, s[70:71]

.LBB0_799:
	v_exp_f32_e32 v159, v96
	v_exp_f32_e32 v161, v97
	v_exp_f32_e32 v157, v98
	v_exp_f32_e32 v160, v99
	v_exp_f32_e32 v155, v100
	v_exp_f32_e32 v158, v101
	v_exp_f32_e32 v154, v102
	v_exp_f32_e32 v156, v103
	v_exp_f32_e32 v151, v104
	v_exp_f32_e32 v153, v105
	v_exp_f32_e32 v149, v106
	v_exp_f32_e32 v152, v107
	v_exp_f32_e32 v147, v108
	v_exp_f32_e32 v150, v109
	v_exp_f32_e32 v146, v110
	v_exp_f32_e32 v148, v111
	v_fma_f32 v80, v193, v179, v195
	v_fma_f32 v179, v80, v198, v199
	s_cmp_gt_u32 s55, 32
	s_waitcnt vmcnt(4) lgkmcnt(0)
	s_barrier
	s_cbranch_scc1 .LBB0_803
	s_add_i32 s55, s55, 2
	v_mov_b32_e32 v193, v197
	ds_read_b128 v[80:83], v130 offset:50176
	ds_read_b128 v[84:87], v130 offset:58368
	ds_read_b128 v[196:199], v131 offset:50176
	ds_read_b128 v[200:203], v131 offset:58368
	s_waitcnt lgkmcnt(2)
	v_mfma_f32_32x32x16_bf16 v[96:111], v[80:83], v[122:125], 0
	v_exp_f32_e32 v204, v72
	v_exp_f32_e32 v205, v73
	v_exp_f32_e32 v206, v74
	v_exp_f32_e32 v207, v75
	v_exp_f32_e32 v208, v76
	v_exp_f32_e32 v209, v77
	v_mfma_f32_32x32x16_bf16 v[80:95], v[84:87], v[122:125], 0
	ds_read_b128 v[138:141], v132 offset:50176
	ds_read_b128 v[142:145], v132 offset:58368
	v_exp_f32_e32 v210, v78
	v_exp_f32_e32 v79, v79
	s_waitcnt lgkmcnt(2)
	v_mfma_f32_32x32x16_bf16 v[96:111], v[196:199], v[126:129], v[96:111]
	v_mfma_f32_32x32x16_bf16 v[80:95], v[200:203], v[126:129], v[80:95]
	ds_read_b128 v[196:199], v133 offset:50176
	ds_read_b128 v[200:203], v133 offset:58368
	s_waitcnt lgkmcnt(2)
	v_mfma_f32_32x32x16_bf16 v[96:111], v[138:141], v[118:121], v[96:111]
	v_mfma_f32_32x32x16_bf16 v[80:95], v[142:145], v[118:121], v[80:95]
	v_exp_f32_e32 v180, v64
	v_add_f32_e32 v64, v161, v159
	v_add_f32_e32 v195, v157, v160
	v_add_f32_e32 v64, v155, v64
	v_add_f32_e32 v195, v158, v195
	v_add_f32_e32 v64, v154, v64
	v_add_f32_e32 v195, v156, v195
	v_add_f32_e32 v64, v151, v64
	v_add_f32_e32 v195, v153, v195
	v_add_f32_e32 v64, v149, v64
	v_add_f32_e32 v195, v152, v195
	v_add_f32_e32 v64, v147, v64
	s_waitcnt lgkmcnt(0)
	v_mfma_f32_32x32x16_bf16 v[96:111], v[196:199], v[114:117], v[96:111]
	v_exp_f32_e32 v197, v65
	v_add_f32_e32 v195, v150, v195
	v_exp_f32_e32 v198, v66
	v_add_f32_e32 v64, v146, v64
	v_exp_f32_e32 v199, v67
	v_add_f32_e32 v195, v148, v195
	v_add_f32_e32 v64, v180, v64
	v_mfma_f32_32x32x16_bf16 v[80:95], v[200:203], v[114:117], v[80:95]
	v_exp_f32_e32 v200, v68
	v_exp_f32_e32 v201, v69
	v_add_f32_e32 v195, v197, v195
	v_exp_f32_e32 v202, v70
	v_add_f32_e32 v64, v198, v64
	v_exp_f32_e32 v203, v71
	v_add_f32_e32 v195, v199, v195
	v_add_f32_e32 v64, v200, v64
	v_add_f32_e32 v195, v201, v195
	v_add_f32_e32 v64, v202, v64
	v_add_f32_e32 v195, v203, v195
	v_add_f32_e32 v64, v204, v64
	v_add_f32_e32 v195, v205, v195
	v_add_f32_e32 v64, v206, v64
	v_add_f32_e32 v195, v207, v195
	v_add_f32_e32 v64, v208, v64
	v_add_f32_e32 v195, v209, v195
	v_add_f32_e32 v64, v210, v64
	v_add_f32_e32 v195, v79, v195
	v_add_f32_e32 v195, v195, v64
	v_cvt_pk_bf16_f32 v64, v159, v161
	v_cvt_pk_bf16_f32 v65, v157, v160
	v_cvt_pk_bf16_f32 v66, v155, v158
	v_cvt_pk_bf16_f32 v67, v154, v156
	v_cvt_pk_bf16_f32 v68, v151, v153
	v_cvt_pk_bf16_f32 v69, v149, v152
	v_cvt_pk_bf16_f32 v70, v147, v150
	v_cvt_pk_bf16_f32 v71, v146, v148
	v_cvt_pk_bf16_f32 v72, v180, v197
	v_cvt_pk_bf16_f32 v73, v198, v199
	v_cvt_pk_bf16_f32 v74, v200, v201
	v_cvt_pk_bf16_f32 v75, v202, v203
	v_cvt_pk_bf16_f32 v76, v204, v205
	v_cvt_pk_bf16_f32 v77, v206, v207
	v_cvt_pk_bf16_f32 v78, v208, v209
	v_cvt_pk_bf16_f32 v79, v210, v79
	s_add_i32 m0, s84, 0x4400
	s_add_u32 s66, s78, s65
	s_addc_u32 s67, s79, 0
	global_load_lds_dwordx4 v185, s[66:67]
	s_add_i32 m0, s84, 0x6400
	s_add_i32 s64, s65, 0x60000
	global_load_lds_dwordx4 v184, s[66:67]
	s_add_i32 m0, s84, 0x14400
	s_add_u32 s70, s80, s64
	s_addc_u32 s71, s81, 0
	global_load_lds_dwordx4 v183, s[70:71]
	s_add_i32 m0, s84, 0x16400
	s_mov_b32 s65, s64
	global_load_lds_dwordx4 v182, s[70:71]
	ds_read_b64_tr_b16 v[198:199], v192 offset:33792
	ds_read_b64_tr_b16 v[200:201], v192 offset:35840
	ds_read_b64_tr_b16 v[202:203], v192 offset:37888
	ds_read_b64_tr_b16 v[204:205], v192 offset:39936
	ds_read_b64_tr_b16 v[206:207], v192 offset:41984
	ds_read_b64_tr_b16 v[208:209], v192 offset:44032
	ds_read_b64_tr_b16 v[222:223], v192 offset:46080
	ds_read_b64_tr_b16 v[224:225], v192 offset:48128
	s_waitcnt lgkmcnt(0)
	v_mfma_f32_32x32x16_bf16 v[0:15], v[64:67], v[198:201], v[0:15]
	ds_read_b64_tr_b16 v[198:199], v192 offset:34304
	ds_read_b64_tr_b16 v[200:201], v192 offset:36352
	ds_read_b64_tr_b16 v[138:139], v192 offset:42496
	ds_read_b64_tr_b16 v[140:141], v192 offset:44544
	v_mfma_f32_32x32x16_bf16 v[0:15], v[68:71], v[202:205], v[0:15]
	ds_read_b64_tr_b16 v[202:203], v192 offset:38400
	ds_read_b64_tr_b16 v[204:205], v192 offset:40448
	ds_read_b64_tr_b16 v[142:143], v192 offset:46592
	ds_read_b64_tr_b16 v[144:145], v192 offset:48640
	v_mfma_f32_32x32x16_bf16 v[0:15], v[72:75], v[206:209], v[0:15]
	v_mfma_f32_32x32x16_bf16 v[0:15], v[76:79], v[222:225], v[0:15]
	s_waitcnt lgkmcnt(0)
	v_mfma_f32_32x32x16_bf16 v[48:63], v[64:67], v[198:201], v[48:63]
	ds_read_b64_tr_b16 v[198:199], v192 offset:34816
	ds_read_b64_tr_b16 v[200:201], v192 offset:36864
	ds_read_b64_tr_b16 v[206:207], v192 offset:43008
	ds_read_b64_tr_b16 v[208:209], v192 offset:45056
	v_mfma_f32_32x32x16_bf16 v[48:63], v[68:71], v[202:205], v[48:63]
	ds_read_b64_tr_b16 v[202:203], v192 offset:38912
	ds_read_b64_tr_b16 v[204:205], v192 offset:40960
	ds_read_b64_tr_b16 v[222:223], v192 offset:47104
	ds_read_b64_tr_b16 v[224:225], v192 offset:49152
	v_mfma_f32_32x32x16_bf16 v[48:63], v[72:75], v[138:141], v[48:63]
	v_mfma_f32_32x32x16_bf16 v[48:63], v[76:79], v[142:145], v[48:63]
	s_waitcnt lgkmcnt(0)
	v_mfma_f32_32x32x16_bf16 v[32:47], v[64:67], v[198:201], v[32:47]
	ds_read_b64_tr_b16 v[198:199], v192 offset:35328
	ds_read_b64_tr_b16 v[200:201], v192 offset:37376
	ds_read_b64_tr_b16 v[138:139], v192 offset:43520
	ds_read_b64_tr_b16 v[140:141], v192 offset:45568
	v_mfma_f32_32x32x16_bf16 v[32:47], v[68:71], v[202:205], v[32:47]
	ds_read_b64_tr_b16 v[202:203], v192 offset:39424
	ds_read_b64_tr_b16 v[204:205], v192 offset:41472
	ds_read_b64_tr_b16 v[142:143], v192 offset:47616
	ds_read_b64_tr_b16 v[144:145], v192 offset:49664
	v_mfma_f32_32x32x16_bf16 v[32:47], v[72:75], v[206:209], v[32:47]
	v_mfma_f32_32x32x16_bf16 v[32:47], v[76:79], v[222:225], v[32:47]
	s_waitcnt lgkmcnt(0)
	v_mfma_f32_32x32x16_bf16 v[16:31], v[64:67], v[198:201], v[16:31]
	v_max_f32_e32 v64, v96, v97
	v_max3_f32 v65, v80, v81, v82
	v_max3_f32 v64, v64, v98, v99
	v_max3_f32 v65, v65, v83, v84
	v_max3_f32 v64, v64, v100, v101
	v_mfma_f32_32x32x16_bf16 v[16:31], v[68:71], v[202:205], v[16:31]
	v_max3_f32 v65, v65, v85, v86
	v_max3_f32 v64, v64, v102, v103
	v_max3_f32 v65, v65, v87, v88
	v_max3_f32 v64, v64, v104, v105
	v_max3_f32 v65, v65, v89, v90
	v_max3_f32 v64, v64, v106, v107
	v_max3_f32 v65, v65, v91, v92
	v_mfma_f32_32x32x16_bf16 v[16:31], v[72:75], v[138:141], v[16:31]
	v_max3_f32 v64, v64, v108, v109
	v_max3_f32 v65, v65, v93, v94
	v_max3_f32 v64, v64, v110, v111
	v_max3_f32 v64, v64, v65, v95
	v_mov_b32_e32 v198, 1.0
	v_mfma_f32_32x32x16_bf16 v[16:31], v[76:79], v[142:145], v[16:31]
	v_cmp_ge_f32_e64 s[0:1], s56, v64
	s_cmp_eq_u64 s[0:1], exec
	s_cbranch_scc1 .Lc1_792
	s_branch .Lc1_801

.Lc1_792:
	v_exp_f32_e32 v197, v96
	v_exp_f32_e32 v208, v97
	v_exp_f32_e32 v209, v98
	v_exp_f32_e32 v210, v99
	v_exp_f32_e32 v211, v100
	v_exp_f32_e32 v220, v101
	v_exp_f32_e32 v221, v102
	v_exp_f32_e32 v222, v103
	v_exp_f32_e32 v223, v104
	v_exp_f32_e32 v224, v105
	v_exp_f32_e32 v225, v106
	v_exp_f32_e32 v226, v107
	v_exp_f32_e32 v227, v108
	v_exp_f32_e32 v228, v109
	v_exp_f32_e32 v229, v110
	v_exp_f32_e32 v230, v111
	s_waitcnt vmcnt(4) lgkmcnt(0)
	s_barrier
	ds_read_b128 v[64:67], v134 offset:33792
	ds_read_b128 v[68:71], v134 offset:41984
	ds_read_b128 v[200:203], v135 offset:33792
	ds_read_b128 v[204:207], v135 offset:41984
	v_exp_f32_e32 v231, v87
	s_waitcnt lgkmcnt(2)
	v_mfma_f32_32x32x16_bf16 v[96:111], v[64:67], v[122:125], 0
	v_exp_f32_e32 v232, v88
	v_exp_f32_e32 v233, v89
	v_exp_f32_e32 v234, v90
	v_exp_f32_e32 v235, v91
	v_exp_f32_e32 v236, v92
	v_exp_f32_e32 v237, v93
	v_exp_f32_e32 v238, v94
	v_mfma_f32_32x32x16_bf16 v[64:79], v[68:71], v[122:125], 0
	ds_read_b128 v[138:141], v136 offset:33792
	ds_read_b128 v[142:145], v136 offset:41984
	v_exp_f32_e32 v95, v95
	s_waitcnt lgkmcnt(2)
	v_mfma_f32_32x32x16_bf16 v[96:111], v[200:203], v[126:129], v[96:111]
	v_mfma_f32_32x32x16_bf16 v[64:79], v[204:207], v[126:129], v[64:79]
	ds_read_b128 v[200:203], v137 offset:33792
	ds_read_b128 v[204:207], v137 offset:41984
	s_waitcnt lgkmcnt(2)
	v_mfma_f32_32x32x16_bf16 v[96:111], v[138:141], v[118:121], v[96:111]
	v_mfma_f32_32x32x16_bf16 v[64:79], v[142:145], v[118:121], v[64:79]
	s_waitcnt lgkmcnt(0)
	v_mfma_f32_32x32x16_bf16 v[96:111], v[200:203], v[114:117], v[96:111]
	v_exp_f32_e32 v201, v80
	v_add_f32_e32 v80, v208, v197
	v_add_f32_e32 v199, v209, v210
	v_add_f32_e32 v80, v211, v80
	v_add_f32_e32 v199, v220, v199
	v_add_f32_e32 v80, v221, v80
	v_add_f32_e32 v199, v222, v199
	v_add_f32_e32 v80, v223, v80
	v_add_f32_e32 v199, v224, v199
	v_add_f32_e32 v80, v225, v80
	v_add_f32_e32 v199, v226, v199
	v_add_f32_e32 v80, v227, v80
	v_exp_f32_e32 v202, v81
	v_add_f32_e32 v199, v228, v199
	v_exp_f32_e32 v203, v82
	v_add_f32_e32 v80, v229, v80
	v_mfma_f32_32x32x16_bf16 v[64:79], v[204:207], v[114:117], v[64:79]
	v_exp_f32_e32 v204, v83
	v_add_f32_e32 v199, v230, v199
	v_exp_f32_e32 v205, v84
	v_add_f32_e32 v80, v201, v80
	v_exp_f32_e32 v206, v85
	v_add_f32_e32 v199, v202, v199
	v_exp_f32_e32 v207, v86
	v_add_f32_e32 v80, v203, v80
	v_add_f32_e32 v199, v204, v199
	v_add_f32_e32 v80, v205, v80
	v_add_f32_e32 v199, v206, v199
	v_add_f32_e32 v80, v207, v80
	v_add_f32_e32 v199, v231, v199
	v_add_f32_e32 v80, v232, v80
	v_add_f32_e32 v199, v233, v199
	v_add_f32_e32 v80, v234, v80
	v_add_f32_e32 v199, v235, v199
	v_add_f32_e32 v80, v236, v80
	v_add_f32_e32 v199, v237, v199
	v_add_f32_e32 v80, v238, v80
	v_add_f32_e32 v199, v95, v199
	v_add_f32_e32 v199, v199, v80
	v_cvt_pk_bf16_f32 v80, v197, v208
	v_cvt_pk_bf16_f32 v81, v209, v210
	v_cvt_pk_bf16_f32 v82, v211, v220
	v_cvt_pk_bf16_f32 v83, v221, v222
	v_cvt_pk_bf16_f32 v84, v223, v224
	v_cvt_pk_bf16_f32 v85, v225, v226
	v_cvt_pk_bf16_f32 v86, v227, v228
	v_cvt_pk_bf16_f32 v87, v229, v230
	v_cvt_pk_bf16_f32 v88, v201, v202
	v_cvt_pk_bf16_f32 v89, v203, v204
	v_cvt_pk_bf16_f32 v90, v205, v206
	v_cvt_pk_bf16_f32 v91, v207, v231
	v_cvt_pk_bf16_f32 v92, v232, v233
	v_cvt_pk_bf16_f32 v93, v234, v235
	v_cvt_pk_bf16_f32 v94, v236, v237
	v_cvt_pk_bf16_f32 v95, v238, v95
	s_add_i32 m0, s84, 0x8400
	s_add_u32 s66, s78, s65
	s_addc_u32 s67, s79, 0
	global_load_lds_dwordx4 v185, s[66:67]
	s_add_i32 m0, s84, 0xa400
	s_add_i32 s64, s65, 0x60000
	global_load_lds_dwordx4 v184, s[66:67]
	s_cmp_eq_u32 s55, 29
	s_cselect_b32 s64, s89, s64
	s_add_i32 m0, s84, 0xc400
	s_add_u32 s70, s80, s64
	s_addc_u32 s71, s81, 0
	global_load_lds_dwordx4 v183, s[70:71]
	s_add_i32 m0, s84, 0xe400
	s_mov_b32 s65, s64
	global_load_lds_dwordx4 v182, s[70:71]

.Lc1_799:
	v_exp_f32_e32 v159, v96
	v_exp_f32_e32 v161, v97
	v_exp_f32_e32 v157, v98
	v_exp_f32_e32 v160, v99
	v_exp_f32_e32 v155, v100
	v_exp_f32_e32 v158, v101
	v_exp_f32_e32 v154, v102
	v_exp_f32_e32 v156, v103
	v_exp_f32_e32 v151, v104
	v_exp_f32_e32 v153, v105
	v_exp_f32_e32 v149, v106
	v_exp_f32_e32 v152, v107
	v_exp_f32_e32 v147, v108
	v_exp_f32_e32 v150, v109
	v_exp_f32_e32 v146, v110
	v_exp_f32_e32 v148, v111
	v_fma_f32 v80, v193, v179, v195
	v_fma_f32 v179, v80, v198, v199
	s_cmp_gt_u32 s55, 32
	s_waitcnt vmcnt(4) lgkmcnt(0)
	s_barrier
	s_cbranch_scc1 .LBB0_803
	s_add_i32 s55, s55, 2
	v_mov_b32_e32 v193, v197
	ds_read_b128 v[80:83], v134 offset:50176
	ds_read_b128 v[84:87], v134 offset:58368
	ds_read_b128 v[196:199], v135 offset:50176
	ds_read_b128 v[200:203], v135 offset:58368
	s_waitcnt lgkmcnt(2)
	v_mfma_f32_32x32x16_bf16 v[96:111], v[80:83], v[122:125], 0
	v_exp_f32_e32 v204, v72
	v_exp_f32_e32 v205, v73
	v_exp_f32_e32 v206, v74
	v_exp_f32_e32 v207, v75
	v_exp_f32_e32 v208, v76
	v_exp_f32_e32 v209, v77
	v_mfma_f32_32x32x16_bf16 v[80:95], v[84:87], v[122:125], 0
	ds_read_b128 v[138:141], v136 offset:50176
	ds_read_b128 v[142:145], v136 offset:58368
	v_exp_f32_e32 v210, v78
	v_exp_f32_e32 v79, v79
	s_waitcnt lgkmcnt(2)
	v_mfma_f32_32x32x16_bf16 v[96:111], v[196:199], v[126:129], v[96:111]
	v_mfma_f32_32x32x16_bf16 v[80:95], v[200:203], v[126:129], v[80:95]
	ds_read_b128 v[196:199], v137 offset:50176
	ds_read_b128 v[200:203], v137 offset:58368
	s_waitcnt lgkmcnt(2)
	v_mfma_f32_32x32x16_bf16 v[96:111], v[138:141], v[118:121], v[96:111]
	v_mfma_f32_32x32x16_bf16 v[80:95], v[142:145], v[118:121], v[80:95]
	v_exp_f32_e32 v180, v64
	v_add_f32_e32 v64, v161, v159
	v_add_f32_e32 v195, v157, v160
	v_add_f32_e32 v64, v155, v64
	v_add_f32_e32 v195, v158, v195
	v_add_f32_e32 v64, v154, v64
	v_add_f32_e32 v195, v156, v195
	v_add_f32_e32 v64, v151, v64
	v_add_f32_e32 v195, v153, v195
	v_add_f32_e32 v64, v149, v64
	v_add_f32_e32 v195, v152, v195
	v_add_f32_e32 v64, v147, v64
	s_waitcnt lgkmcnt(0)
	v_mfma_f32_32x32x16_bf16 v[96:111], v[196:199], v[114:117], v[96:111]
	v_exp_f32_e32 v197, v65
	v_add_f32_e32 v195, v150, v195
	v_exp_f32_e32 v198, v66
	v_add_f32_e32 v64, v146, v64
	v_exp_f32_e32 v199, v67
	v_add_f32_e32 v195, v148, v195
	v_add_f32_e32 v64, v180, v64
	v_mfma_f32_32x32x16_bf16 v[80:95], v[200:203], v[114:117], v[80:95]
	v_exp_f32_e32 v200, v68
	v_exp_f32_e32 v201, v69
	v_add_f32_e32 v195, v197, v195
	v_exp_f32_e32 v202, v70
	v_add_f32_e32 v64, v198, v64
	v_exp_f32_e32 v203, v71
	v_add_f32_e32 v195, v199, v195
	v_add_f32_e32 v64, v200, v64
	v_add_f32_e32 v195, v201, v195
	v_add_f32_e32 v64, v202, v64
	v_add_f32_e32 v195, v203, v195
	v_add_f32_e32 v64, v204, v64
	v_add_f32_e32 v195, v205, v195
	v_add_f32_e32 v64, v206, v64
	v_add_f32_e32 v195, v207, v195
	v_add_f32_e32 v64, v208, v64
	v_add_f32_e32 v195, v209, v195
	v_add_f32_e32 v64, v210, v64
	v_add_f32_e32 v195, v79, v195
	v_add_f32_e32 v195, v195, v64
	v_cvt_pk_bf16_f32 v64, v159, v161
	v_cvt_pk_bf16_f32 v65, v157, v160
	v_cvt_pk_bf16_f32 v66, v155, v158
	v_cvt_pk_bf16_f32 v67, v154, v156
	v_cvt_pk_bf16_f32 v68, v151, v153
	v_cvt_pk_bf16_f32 v69, v149, v152
	v_cvt_pk_bf16_f32 v70, v147, v150
	v_cvt_pk_bf16_f32 v71, v146, v148
	v_cvt_pk_bf16_f32 v72, v180, v197
	v_cvt_pk_bf16_f32 v73, v198, v199
	v_cvt_pk_bf16_f32 v74, v200, v201
	v_cvt_pk_bf16_f32 v75, v202, v203
	v_cvt_pk_bf16_f32 v76, v204, v205
	v_cvt_pk_bf16_f32 v77, v206, v207
	v_cvt_pk_bf16_f32 v78, v208, v209
	v_cvt_pk_bf16_f32 v79, v210, v79
	s_add_i32 m0, s84, 0x400
	s_add_u32 s66, s78, s65
	s_addc_u32 s67, s79, 0
	global_load_lds_dwordx4 v185, s[66:67]
	s_add_i32 m0, s84, 0x2400
	s_add_i32 s64, s65, 0x60000
	global_load_lds_dwordx4 v184, s[66:67]
	s_add_i32 m0, s84, 0x10400
	s_add_u32 s70, s80, s64
	s_addc_u32 s71, s81, 0
	global_load_lds_dwordx4 v183, s[70:71]
	s_add_i32 m0, s84, 0x12400
	s_mov_b32 s65, s64
	global_load_lds_dwordx4 v182, s[70:71]
	ds_read_b64_tr_b16 v[198:199], v192 offset:17408
	ds_read_b64_tr_b16 v[200:201], v192 offset:19456
	ds_read_b64_tr_b16 v[202:203], v192 offset:21504
	ds_read_b64_tr_b16 v[204:205], v192 offset:23552
	ds_read_b64_tr_b16 v[206:207], v192 offset:25600
	ds_read_b64_tr_b16 v[208:209], v192 offset:27648
	ds_read_b64_tr_b16 v[222:223], v192 offset:29696
	ds_read_b64_tr_b16 v[224:225], v192 offset:31744
	s_waitcnt lgkmcnt(0)
	v_mfma_f32_32x32x16_bf16 v[0:15], v[64:67], v[198:201], v[0:15]
	ds_read_b64_tr_b16 v[198:199], v192 offset:17920
	ds_read_b64_tr_b16 v[200:201], v192 offset:19968
	ds_read_b64_tr_b16 v[138:139], v192 offset:26112
	ds_read_b64_tr_b16 v[140:141], v192 offset:28160
	v_mfma_f32_32x32x16_bf16 v[0:15], v[68:71], v[202:205], v[0:15]
	ds_read_b64_tr_b16 v[202:203], v192 offset:22016
	ds_read_b64_tr_b16 v[204:205], v192 offset:24064
	ds_read_b64_tr_b16 v[142:143], v192 offset:30208
	ds_read_b64_tr_b16 v[144:145], v192 offset:32256
	v_mfma_f32_32x32x16_bf16 v[0:15], v[72:75], v[206:209], v[0:15]
	v_mfma_f32_32x32x16_bf16 v[0:15], v[76:79], v[222:225], v[0:15]
	s_waitcnt lgkmcnt(0)
	v_mfma_f32_32x32x16_bf16 v[48:63], v[64:67], v[198:201], v[48:63]
	ds_read_b64_tr_b16 v[198:199], v192 offset:18432
	ds_read_b64_tr_b16 v[200:201], v192 offset:20480
	ds_read_b64_tr_b16 v[206:207], v192 offset:26624
	ds_read_b64_tr_b16 v[208:209], v192 offset:28672
	v_mfma_f32_32x32x16_bf16 v[48:63], v[68:71], v[202:205], v[48:63]
	ds_read_b64_tr_b16 v[202:203], v192 offset:22528
	ds_read_b64_tr_b16 v[204:205], v192 offset:24576
	ds_read_b64_tr_b16 v[222:223], v192 offset:30720
	ds_read_b64_tr_b16 v[224:225], v192 offset:32768
	v_mfma_f32_32x32x16_bf16 v[48:63], v[72:75], v[138:141], v[48:63]
	v_mfma_f32_32x32x16_bf16 v[48:63], v[76:79], v[142:145], v[48:63]
	s_waitcnt lgkmcnt(0)
	v_mfma_f32_32x32x16_bf16 v[32:47], v[64:67], v[198:201], v[32:47]
	ds_read_b64_tr_b16 v[198:199], v192 offset:18944
	ds_read_b64_tr_b16 v[200:201], v192 offset:20992
	ds_read_b64_tr_b16 v[138:139], v192 offset:27136
	ds_read_b64_tr_b16 v[140:141], v192 offset:29184
	v_mfma_f32_32x32x16_bf16 v[32:47], v[68:71], v[202:205], v[32:47]
	ds_read_b64_tr_b16 v[202:203], v192 offset:23040
	ds_read_b64_tr_b16 v[204:205], v192 offset:25088
	ds_read_b64_tr_b16 v[142:143], v192 offset:31232
	ds_read_b64_tr_b16 v[144:145], v192 offset:33280
	v_mfma_f32_32x32x16_bf16 v[32:47], v[72:75], v[206:209], v[32:47]
	v_mfma_f32_32x32x16_bf16 v[32:47], v[76:79], v[222:225], v[32:47]
	s_waitcnt lgkmcnt(0)
	v_mfma_f32_32x32x16_bf16 v[16:31], v[64:67], v[198:201], v[16:31]
	v_max_f32_e32 v64, v96, v97
	v_max3_f32 v65, v80, v81, v82
	v_max3_f32 v64, v64, v98, v99
	v_max3_f32 v65, v65, v83, v84
	v_max3_f32 v64, v64, v100, v101
	v_mfma_f32_32x32x16_bf16 v[16:31], v[68:71], v[202:205], v[16:31]
	v_max3_f32 v65, v65, v85, v86
	v_max3_f32 v64, v64, v102, v103
	v_max3_f32 v65, v65, v87, v88
	v_max3_f32 v64, v64, v104, v105
	v_max3_f32 v65, v65, v89, v90
	v_max3_f32 v64, v64, v106, v107
	v_max3_f32 v65, v65, v91, v92
	v_mfma_f32_32x32x16_bf16 v[16:31], v[72:75], v[138:141], v[16:31]
	v_max3_f32 v64, v64, v108, v109
	v_max3_f32 v65, v65, v93, v94
	v_max3_f32 v64, v64, v110, v111
	v_max3_f32 v64, v64, v65, v95
	v_mov_b32_e32 v198, 1.0
	v_mfma_f32_32x32x16_bf16 v[16:31], v[76:79], v[142:145], v[16:31]
	v_cmp_ge_f32_e64 s[0:1], s56, v64
	s_cmp_eq_u64 s[0:1], exec
	s_cbranch_scc1 .Lc2_792
	s_branch .Lc2_801

.Lc2_792:
	v_exp_f32_e32 v197, v96
	v_exp_f32_e32 v208, v97
	v_exp_f32_e32 v209, v98
	v_exp_f32_e32 v210, v99
	v_exp_f32_e32 v211, v100
	v_exp_f32_e32 v220, v101
	v_exp_f32_e32 v221, v102
	v_exp_f32_e32 v222, v103
	v_exp_f32_e32 v223, v104
	v_exp_f32_e32 v224, v105
	v_exp_f32_e32 v225, v106
	v_exp_f32_e32 v226, v107
	v_exp_f32_e32 v227, v108
	v_exp_f32_e32 v228, v109
	v_exp_f32_e32 v229, v110
	v_exp_f32_e32 v230, v111
	s_waitcnt vmcnt(4) lgkmcnt(0)
	s_barrier
	ds_read_b128 v[64:67], v130 offset:50176
	ds_read_b128 v[68:71], v130 offset:58368
	ds_read_b128 v[200:203], v131 offset:50176
	ds_read_b128 v[204:207], v131 offset:58368
	v_exp_f32_e32 v231, v87
	s_waitcnt lgkmcnt(2)
	v_mfma_f32_32x32x16_bf16 v[96:111], v[64:67], v[122:125], 0
	v_exp_f32_e32 v232, v88
	v_exp_f32_e32 v233, v89
	v_exp_f32_e32 v234, v90
	v_exp_f32_e32 v235, v91
	v_exp_f32_e32 v236, v92
	v_exp_f32_e32 v237, v93
	v_exp_f32_e32 v238, v94
	v_mfma_f32_32x32x16_bf16 v[64:79], v[68:71], v[122:125], 0
	ds_read_b128 v[138:141], v132 offset:50176
	ds_read_b128 v[142:145], v132 offset:58368
	v_exp_f32_e32 v95, v95
	s_waitcnt lgkmcnt(2)
	v_mfma_f32_32x32x16_bf16 v[96:111], v[200:203], v[126:129], v[96:111]
	v_mfma_f32_32x32x16_bf16 v[64:79], v[204:207], v[126:129], v[64:79]
	ds_read_b128 v[200:203], v133 offset:50176
	ds_read_b128 v[204:207], v133 offset:58368
	s_waitcnt lgkmcnt(2)
	v_mfma_f32_32x32x16_bf16 v[96:111], v[138:141], v[118:121], v[96:111]
	v_mfma_f32_32x32x16_bf16 v[64:79], v[142:145], v[118:121], v[64:79]
	s_waitcnt lgkmcnt(0)
	v_mfma_f32_32x32x16_bf16 v[96:111], v[200:203], v[114:117], v[96:111]
	v_exp_f32_e32 v201, v80
	v_add_f32_e32 v80, v208, v197
	v_add_f32_e32 v199, v209, v210
	v_add_f32_e32 v80, v211, v80
	v_add_f32_e32 v199, v220, v199
	v_add_f32_e32 v80, v221, v80
	v_add_f32_e32 v199, v222, v199
	v_add_f32_e32 v80, v223, v80
	v_add_f32_e32 v199, v224, v199
	v_add_f32_e32 v80, v225, v80
	v_add_f32_e32 v199, v226, v199
	v_add_f32_e32 v80, v227, v80
	v_exp_f32_e32 v202, v81
	v_add_f32_e32 v199, v228, v199
	v_exp_f32_e32 v203, v82
	v_add_f32_e32 v80, v229, v80
	v_mfma_f32_32x32x16_bf16 v[64:79], v[204:207], v[114:117], v[64:79]
	v_exp_f32_e32 v204, v83
	v_add_f32_e32 v199, v230, v199
	v_exp_f32_e32 v205, v84
	v_add_f32_e32 v80, v201, v80
	v_exp_f32_e32 v206, v85
	v_add_f32_e32 v199, v202, v199
	v_exp_f32_e32 v207, v86
	v_add_f32_e32 v80, v203, v80
	v_add_f32_e32 v199, v204, v199
	v_add_f32_e32 v80, v205, v80
	v_add_f32_e32 v199, v206, v199
	v_add_f32_e32 v80, v207, v80
	v_add_f32_e32 v199, v231, v199
	v_add_f32_e32 v80, v232, v80
	v_add_f32_e32 v199, v233, v199
	v_add_f32_e32 v80, v234, v80
	v_add_f32_e32 v199, v235, v199
	v_add_f32_e32 v80, v236, v80
	v_add_f32_e32 v199, v237, v199
	v_add_f32_e32 v80, v238, v80
	v_add_f32_e32 v199, v95, v199
	v_add_f32_e32 v199, v199, v80
	v_cvt_pk_bf16_f32 v80, v197, v208
	v_cvt_pk_bf16_f32 v81, v209, v210
	v_cvt_pk_bf16_f32 v82, v211, v220
	v_cvt_pk_bf16_f32 v83, v221, v222
	v_cvt_pk_bf16_f32 v84, v223, v224
	v_cvt_pk_bf16_f32 v85, v225, v226
	v_cvt_pk_bf16_f32 v86, v227, v228
	v_cvt_pk_bf16_f32 v87, v229, v230
	v_cvt_pk_bf16_f32 v88, v201, v202
	v_cvt_pk_bf16_f32 v89, v203, v204
	v_cvt_pk_bf16_f32 v90, v205, v206
	v_cvt_pk_bf16_f32 v91, v207, v231
	v_cvt_pk_bf16_f32 v92, v232, v233
	v_cvt_pk_bf16_f32 v93, v234, v235
	v_cvt_pk_bf16_f32 v94, v236, v237
	v_cvt_pk_bf16_f32 v95, v238, v95
	s_add_i32 m0, s84, 0x4400
	s_add_u32 s66, s78, s65
	s_addc_u32 s67, s79, 0
	global_load_lds_dwordx4 v185, s[66:67]
	s_add_i32 m0, s84, 0x6400
	s_add_i32 s64, s65, 0x60000
	global_load_lds_dwordx4 v184, s[66:67]
	s_cmp_eq_u32 s55, 29
	s_cselect_b32 s64, s89, s64
	s_add_i32 m0, s84, 0x14400
	s_add_u32 s70, s80, s64
	s_addc_u32 s71, s81, 0
	global_load_lds_dwordx4 v183, s[70:71]
	s_add_i32 m0, s84, 0x16400
	s_mov_b32 s65, s64
	global_load_lds_dwordx4 v182, s[70:71]
